# mixer A unit start: the vmcnt(0) behind the Q loads removed (covered by the tile loop's counted wait), so Q and first-tile latencies overlap
# baseline (speedup 1.0000x reference)
; __device__ __forceinline__ void mixer_a_phase(const bf16* AQ, const bf16* AK, const bf16* AV  , bf16* O, float* ST, float* ML, const float* rel_bias, LAS unsigned char* lds, int G, int blk, int tid, int lane, int wave) {
;     ...
;         const int i5 = lane & 31, hh = lane >> 5;
;         const size_t tb0 = (size_t)b * SEQ;
;         const bf16* Kb = AK + tb0 * 512 + h * 64; const bf16* Vb = AV + tb0 * 512 + h * 64;
;         bf16x8 qn[4];
;         { const bf16* qp = AQ + (tb0 + 512 * a + 32 * wave + i5) * 512 + h * 64 + 8 * hh;
; #pragma unroll
;           for (int d0 = 0; d0 < 4; ++d0) qn[d0] = *(const bf16x8*)(qp + 16 * d0); }
.LBB0_357:
	s_ashr_i32 s8, s43, 7
	s_bfe_u32 s1, s43, 0x40003
	s_ashr_i32 s9, s8, 31
	s_lshl_b32 s0, s1, 9
	s_lshl_b64 s[22:23], s[8:9], 13
	s_lshl_b32 s24, s44, 6
	s_lshl_b64 s[10:11], s[8:9], 23
	v_readlane_b32 s8, v255, 9
	v_readlane_b32 s9, v255, 10
	s_add_u32 s8, s8, s10
	s_addc_u32 s9, s9, s11
	s_or_b32 s26, s22, s0
	s_mov_b32 s27, s23
	v_lshl_add_u64 v[4:5], s[26:27], 0, v[138:139]
	v_readlane_b32 s34, v255, 7
	v_lshlrev_b64 v[4:5], 10, v[4:5]
	v_readlane_b32 s35, v255, 8
	s_lshl_b32 s16, s44, 7
	v_mov_b32_e32 v151, v3
	v_lshl_add_u64 v[4:5], s[34:35], 0, v[4:5]
	v_lshl_add_u64 v[4:5], v[4:5], 0, s[16:17]
	v_lshl_add_u64 v[4:5], v[4:5], 0, v[150:151]
	global_load_dwordx4 v[52:55], v[4:5], off
	global_load_dwordx4 v[56:59], v[4:5], off offset:32
	global_load_dwordx4 v[60:63], v[4:5], off offset:64
	global_load_dwordx4 v[64:67], v[4:5], off offset:96
	s_add_u32 s14, s86, s10
	s_addc_u32 s15, s87, s11
	s_add_u32 s28, s14, s16
	s_addc_u32 s29, s15, 0
	s_add_u32 s30, s8, s16
	v_cndmask_b32_e64 v2, 0, 1, s[18:19]
	s_mov_b32 s25, s17
	s_addc_u32 s31, s9, 0
	v_cmp_ne_u32_e64 s[8:9], 1, v2
	s_andn2_b64 vcc, exec, s[18:19]
	s_nop 0
	v_lshlrev_b32_e32 v68, 1, v142
	s_cbranch_vccnz .LBB0_380
	v_mov_b32_e32 v5, s27
	v_or_b32_e32 v4, s26, v140
	v_lshlrev_b64 v[4:5], 10, v[4:5]
	v_mov_b32_e32 v69, v3
	v_add_u32_e32 v162, s0, v207
	v_lshl_add_u64 v[152:153], s[34:35], 0, v[4:5]
	v_lshl_add_u64 v[154:155], s[28:29], 0, v[68:69]
	v_lshl_add_u64 v[156:157], s[30:31], 0, v[68:69]
	v_readlane_b32 s14, v254, 59
